# speedup vs baseline: 1.0153x; 1.0153x over previous
.LBB1_16:
	s_or_b64 exec, exec, s[4:5]
	s_lshl_b32 s3, s2, 2
	v_lshrrev_b32_e32 v14, 6, v0
	s_add_i32 s4, s3, 0xfffff9e4
	v_or_b32_e32 v2, s4, v14
	s_movk_i32 s4, 2500
	v_cmp_gt_i32_e32 vcc, s4, v2
	s_waitcnt lgkmcnt(0)
	s_barrier
	s_and_saveexec_b64 s[6:7], vcc
	s_cbranch_execz .LBB1_21
	s_load_dwordx2 s[4:5], s[0:1], 0x28
	v_and_b32_e32 v1, 15, v0
	v_lshl_or_b32 v2, v2, 4, v1
	v_ashrrev_i32_e32 v3, 31, v2
	v_lshlrev_b64 v[2:3], 9, v[2:3]
	v_and_b32_e32 v66, 48, v0
	v_mov_b32_e32 v67, 0
	s_waitcnt lgkmcnt(0)
	v_lshl_add_u64 v[2:3], s[4:5], 0, v[2:3]
	v_lshl_add_u64 v[16:17], v[2:3], 0, v[66:67]
	global_load_dwordx4 v[38:41], v[16:17], off offset:448
	global_load_dwordx4 v[34:37], v[16:17], off offset:384
	global_load_dwordx4 v[46:49], v[16:17], off offset:320
	global_load_dwordx4 v[42:45], v[16:17], off offset:256
	global_load_dwordx4 v[6:9], v[16:17], off offset:192
	global_load_dwordx4 v[18:21], v[16:17], off offset:128
	global_load_dwordx4 v[2:5], v[16:17], off offset:64
	global_load_dwordx4 v[10:13], v[16:17], off
	s_load_dwordx2 s[8:9], s[0:1], 0x58
	s_load_dwordx2 s[10:11], s[0:1], 0x48
	v_and_b32_e32 v15, 63, v0
	v_lshl_add_u64 v[68:69], s[4:5], 0, v[66:67]
	s_movk_i32 s4, 0x1100
	v_cmp_gt_u32_e32 vcc, 16, v15
	v_mul_u32_u24_e32 v15, 0x110, v1
	v_mul_u32_u24_e32 v17, 0x1100, v14
	v_mad_u32_u24 v22, v14, s4, v15
	v_lshlrev_b32_e32 v16, 4, v1
	v_add_u32_e32 v25, s3, v14
	v_lshlrev_b32_e32 v14, 4, v14
	v_bfe_u32 v80, v0, 4, 2
	v_or_b32_e32 v24, v17, v16
	v_mov_b32_e32 v17, v67
	v_lshl_or_b32 v82, s2, 6, v14
	v_mbcnt_lo_u32_b32 v14, -1, 0
	s_waitcnt lgkmcnt(0)
	v_lshl_add_u64 v[70:71], s[10:11], 0, v[16:17]
	v_or_b32_e32 v17, 4, v80
	v_mbcnt_hi_u32_b32 v84, -1, v14
	v_lshlrev_b32_e32 v23, 3, v80
	v_mul_u32_u24_e32 v16, 0x110, v80
	v_mul_u32_u24_e32 v17, 0x110, v17
	v_and_b32_e32 v14, 64, v84
	v_subrev_u32_e32 v67, 56, v25
	v_or_b32_e32 v81, 0xffff9e40, v1
	s_mov_b64 s[10:11], 0
	s_movk_i32 s3, 992
	v_add_u32_e32 v83, v66, v15
	v_xor_b32_e32 v85, 16, v84
	v_add_u32_e32 v86, 64, v14
	v_xor_b32_e32 v87, 32, v84
	v_add_u32_e32 v88, v22, v23
	v_add_u32_e32 v89, v24, v16
	v_add_u32_e32 v90, v24, v17
	s_movk_i32 s12, 991
	s_waitcnt vmcnt(0)
	s_branch .LBB1_19

.LBB1_19:
	ds_read_b128 v[14:17], v83
	v_cvt_pk_f16_f32 v5, v4, v5
	v_cvt_pk_f16_f32 v4, v2, v3
	v_cvt_pk_f16_f32 v3, v12, v13
	v_cvt_pk_f16_f32 v2, v10, v11
	ds_read_b128 v[10:13], v83 offset:64
	ds_read_b128 v[22:25], v83 offset:4352
	ds_read_b128 v[26:29], v83 offset:4416
	ds_read_b128 v[30:33], v83 offset:8704
	ds_read_b128 v[50:53], v83 offset:8768
	ds_read_b128 v[54:57], v83 offset:13056
	ds_read_b128 v[58:61], v83 offset:13120
	ds_read_b128 v[62:65], v83 offset:17408
	ds_read_b128 v[72:75], v83 offset:17472
	ds_read_b128 v[76:79], v83 offset:21760
	ds_read_b128 v[92:95], v83 offset:21824
	ds_read_b128 v[96:99], v83 offset:26112
	ds_read_b128 v[100:103], v83 offset:26176
	ds_read_b128 v[104:107], v83 offset:30464
	ds_read_b128 v[110:113], v83 offset:30528
	v_add_u32_e32 v91, 0xfffffa1c, v67
	v_cmp_gt_i32_e64 s[4:5], s3, v91
	s_waitcnt lgkmcnt(14)
	v_mfma_f32_16x16x32_f16 v[14:17], v[14:17], v[2:5], 0
	v_cvt_pk_f16_f32 v109, v8, v9
	v_cvt_pk_f16_f32 v108, v6, v7
	v_cvt_pk_f16_f32 v49, v48, v49
	s_waitcnt lgkmcnt(13)
	v_mfma_f32_16x16x32_f16 v[22:25], v[22:25], v[2:5], 0
	v_cvt_pk_f16_f32 v48, v46, v47
	v_cvt_pk_f16_f32 v47, v44, v45
	v_cvt_pk_f16_f32 v46, v42, v43
	s_waitcnt lgkmcnt(11)
	v_mfma_f32_16x16x32_f16 v[30:33], v[30:33], v[2:5], 0
	s_waitcnt lgkmcnt(9)
	v_mfma_f32_16x16x32_f16 v[54:57], v[54:57], v[2:5], 0
	s_waitcnt lgkmcnt(7)
	v_mfma_f32_16x16x32_f16 v[62:65], v[62:65], v[2:5], 0
	s_waitcnt lgkmcnt(5)
	v_mfma_f32_16x16x32_f16 v[76:79], v[76:79], v[2:5], 0
	s_waitcnt lgkmcnt(3)
	v_mfma_f32_16x16x32_f16 v[96:99], v[96:99], v[2:5], 0
	s_waitcnt lgkmcnt(1)
	v_mfma_f32_16x16x32_f16 v[114:117], v[104:107], v[2:5], 0
	v_cndmask_b32_e64 v2, v91, v67, s[4:5]
	v_lshl_or_b32 v2, v2, 4, v1
	v_ashrrev_i32_e32 v3, 31, v2
	v_cvt_pk_f16_f32 v107, v20, v21
	v_cvt_pk_f16_f32 v106, v18, v19
	v_lshlrev_b64 v[2:3], 9, v[2:3]
	v_cmp_lt_i32_e64 s[4:5], v85, v86
	v_mfma_f32_16x16x32_f16 v[122:125], v[26:29], v[106:109], v[22:25]
	s_nop 2
	v_lshl_add_u64 v[22:23], v[68:69], 0, v[2:3]
	v_mfma_f32_16x16x32_f16 v[118:121], v[10:13], v[106:109], v[14:17]
	global_load_dwordx4 v[10:13], v[22:23], off
	global_load_dwordx4 v[2:5], v[22:23], off offset:64
	global_load_dwordx4 v[18:21], v[22:23], off offset:128
	global_load_dwordx4 v[6:9], v[22:23], off offset:192
	global_load_dwordx4 v[26:29], v[22:23], off offset:256
	global_load_dwordx4 v[14:17], v[22:23], off offset:320
	v_mfma_f32_16x16x32_f16 v[50:53], v[50:53], v[106:109], v[30:33]
	s_nop 2
	global_load_dwordx4 v[30:33], v[22:23], off offset:384
	s_nop 0
	global_load_dwordx4 v[22:25], v[22:23], off offset:448
	v_mfma_f32_16x16x32_f16 v[54:57], v[58:61], v[106:109], v[54:57]
	v_mfma_f32_16x16x32_f16 v[58:61], v[72:75], v[106:109], v[62:65]
	ds_read_b128 v[72:75], v83 offset:128
	v_mfma_f32_16x16x32_f16 v[62:65], v[92:95], v[106:109], v[76:79]
	ds_read_b128 v[92:95], v83 offset:4480
	v_mfma_f32_16x16x32_f16 v[76:79], v[100:103], v[106:109], v[96:99]
	ds_read_b128 v[42:45], v83 offset:8832
	ds_read_b128 v[100:103], v83 offset:192
	s_waitcnt lgkmcnt(4)
	v_mfma_f32_16x16x32_f16 v[96:99], v[110:113], v[106:109], v[114:117]
	ds_read_b128 v[104:107], v83 offset:13184
	ds_read_b128 v[108:111], v83 offset:17536
	s_nop 0
	ds_read_b128 v[112:115], v83 offset:4544
	s_waitcnt lgkmcnt(5)
	v_mfma_f32_16x16x32_f16 v[92:95], v[92:95], v[46:49], v[122:125]
	s_nop 2
	ds_read_b128 v[124:127], v83 offset:8896
	v_mfma_f32_16x16x32_f16 v[72:75], v[72:75], v[46:49], v[118:121]
	v_cvt_pk_f16_f32 v123, v40, v41
	v_cvt_pk_f16_f32 v122, v38, v39
	s_nop 0
	ds_read_b128 v[116:119], v83 offset:21888
	s_waitcnt lgkmcnt(6)
	v_mfma_f32_16x16x32_f16 v[42:45], v[42:45], v[46:49], v[50:53]
	v_cvt_pk_f16_f32 v121, v36, v37
	v_cvt_pk_f16_f32 v120, v34, v35
	v_cndmask_b32_e64 v34, v84, v85, s[4:5]
	ds_read_b128 v[50:53], v83 offset:13248
	s_waitcnt lgkmcnt(5)
	v_mfma_f32_16x16x32_f16 v[54:57], v[104:107], v[46:49], v[54:57]
	ds_read_b128 v[104:107], v83 offset:17600
	ds_read_b128 v[128:131], v83 offset:21952
	v_lshlrev_b32_e32 v144, 2, v34
	v_cmp_lt_i32_e64 s[4:5], v87, v86
	s_waitcnt lgkmcnt(6)
	v_mfma_f32_16x16x32_f16 v[58:61], v[108:111], v[46:49], v[58:61]
	ds_read_b128 v[108:111], v83 offset:26240
	ds_read_b128 v[132:135], v83 offset:26304
	ds_read_b128 v[136:139], v83 offset:30592
	ds_read_b128 v[140:143], v83 offset:30656
	v_cndmask_b32_e64 v145, v84, v87, s[4:5]
	v_mfma_f32_16x16x32_f16 v[38:41], v[100:103], v[120:123], v[72:75]
	s_nop 2
	ds_read_b128 v[72:75], v66 offset:52736
	ds_read_b128 v[100:103], v66 offset:52800
	s_waitcnt lgkmcnt(10)
	v_mfma_f32_16x16x32_f16 v[34:37], v[124:127], v[120:123], v[42:45]
	ds_read_b128 v[124:127], v66 offset:52864
	s_waitcnt lgkmcnt(6)
	v_mfma_f32_16x16x32_f16 v[76:79], v[108:111], v[46:49], v[76:79]
	ds_read_b128 v[108:111], v66 offset:52928
	v_mov_b32_e32 v42, v38
	s_nop 2
	v_mov_b32_e32 v43, v34
	v_mfma_f32_16x16x32_f16 v[116:119], v[116:119], v[46:49], v[62:65]
	s_waitcnt lgkmcnt(3)
	v_mov_b32_e32 v44, v72
	s_waitcnt lgkmcnt(1)
	v_mov_b32_e32 v45, v124
	v_pk_fma_f32 v[42:43], v[42:43], v[44:45], 0 op_sel_hi:[1,1,0]
	v_mfma_f32_16x16x32_f16 v[62:65], v[112:115], v[120:123], v[92:95]
	v_mov_b32_e32 v44, v39
	v_mov_b32_e32 v45, v35
	v_mov_b32_e32 v124, v73
	v_mfma_f32_16x16x32_f16 v[54:57], v[50:53], v[120:123], v[54:57]
	v_mov_b32_e32 v50, v74
	v_mov_b32_e32 v51, v126
	v_mov_b32_e32 v52, v41
	v_mfma_f32_16x16x32_f16 v[96:99], v[136:139], v[46:49], v[96:99]
	v_fma_f32 v46, v44, v124, v42
	v_fma_f32 v47, v45, v125, v43
	v_mov_b32_e32 v48, v40
	v_mov_b32_e32 v49, v36
	v_pk_fma_f32 v[50:51], v[48:49], v[50:51], v[46:47]
	v_mov_b32_e32 v53, v37
	v_mov_b32_e32 v126, v75
	v_pk_fma_f32 v[72:73], v[52:53], v[126:127], v[50:51]
	v_mov_b32_e32 v74, v62
	v_mfma_f32_16x16x32_f16 v[50:53], v[132:135], v[120:123], v[76:79]
	v_mov_b32_e32 v75, v54
	s_nop 1
	v_mov_b32_e32 v76, v100
	s_waitcnt lgkmcnt(0)
	v_mov_b32_e32 v77, v108
	v_pk_fma_f32 v[72:73], v[74:75], v[76:77], v[72:73]
	v_mov_b32_e32 v74, v63
	v_mov_b32_e32 v75, v55
	v_mov_b32_e32 v108, v101
	v_pk_fma_f32 v[72:73], v[74:75], v[108:109], v[72:73]
	v_mov_b32_e32 v74, v64
	v_mov_b32_e32 v75, v56
	v_mov_b32_e32 v76, v102
	v_mov_b32_e32 v77, v110
	v_pk_fma_f32 v[72:73], v[74:75], v[76:77], v[72:73]
	v_mov_b32_e32 v74, v65
	v_mov_b32_e32 v75, v57
	v_mov_b32_e32 v110, v103
	v_pk_fma_f32 v[100:101], v[74:75], v[110:111], v[72:73]
	ds_read_b128 v[72:75], v66 offset:52992
	ds_read_b128 v[76:79], v66 offset:53056
	ds_read_b128 v[92:95], v66 offset:53120
	v_mfma_f32_16x16x32_f16 v[42:45], v[104:107], v[120:123], v[58:61]
	v_mov_b32_e32 v105, v50
	s_waitcnt lgkmcnt(2)
	v_mov_b32_e32 v106, v72
	ds_bpermute_b32 v102, v144, v100
	v_mfma_f32_16x16x32_f16 v[58:61], v[140:143], v[120:123], v[96:99]
	s_waitcnt lgkmcnt(1)
	v_mov_b32_e32 v107, v92
	s_nop 0
	v_mov_b32_e32 v104, v42
	v_pk_fma_f32 v[104:105], v[104:105], v[106:107], 0 op_sel_hi:[1,1,0]
	ds_read_b128 v[96:99], v66 offset:53184
	v_mfma_f32_16x16x32_f16 v[46:49], v[128:131], v[120:123], v[116:119]
	v_mov_b32_e32 v106, v43
	v_mov_b32_e32 v107, v51
	v_mov_b32_e32 v92, v73
	v_pk_fma_f32 v[72:73], v[106:107], v[92:93], v[104:105]
	v_mov_b32_e32 v92, v44
	v_mov_b32_e32 v93, v52
	v_mov_b32_e32 v104, v74
	v_mov_b32_e32 v105, v94
	v_pk_fma_f32 v[72:73], v[92:93], v[104:105], v[72:73]
	v_mov_b32_e32 v92, v45
	v_mov_b32_e32 v93, v53
	v_mov_b32_e32 v94, v75
	v_pk_fma_f32 v[72:73], v[92:93], v[94:95], v[72:73]
	v_mov_b32_e32 v74, v46
	v_mov_b32_e32 v75, v58
	v_mov_b32_e32 v92, v76
	s_waitcnt lgkmcnt(0)
	v_mov_b32_e32 v93, v96
	v_pk_fma_f32 v[72:73], v[74:75], v[92:93], v[72:73]
	v_mov_b32_e32 v74, v47
	v_mov_b32_e32 v75, v59
	v_mov_b32_e32 v96, v77
	v_pk_fma_f32 v[72:73], v[74:75], v[96:97], v[72:73]
	v_mov_b32_e32 v74, v48
	v_mov_b32_e32 v75, v60
	v_mov_b32_e32 v76, v78
	v_mov_b32_e32 v77, v98
	v_pk_fma_f32 v[72:73], v[74:75], v[76:77], v[72:73]
	v_mov_b32_e32 v74, v49
	v_mov_b32_e32 v75, v61
	v_mov_b32_e32 v98, v79
	v_pk_fma_f32 v[76:77], v[74:75], v[98:99], v[72:73]
	ds_bpermute_b32 v103, v144, v101
	ds_bpermute_b32 v78, v144, v76
	ds_bpermute_b32 v79, v144, v77
	v_lshlrev_b32_e32 v92, 2, v145
	s_waitcnt lgkmcnt(2)
	v_pk_add_f32 v[72:73], v[100:101], v[102:103]
	ds_bpermute_b32 v74, v92, v72
	s_waitcnt lgkmcnt(1)
	v_pk_add_f32 v[76:77], v[76:77], v[78:79]
	ds_bpermute_b32 v75, v92, v73
	ds_bpermute_b32 v78, v92, v76
	ds_bpermute_b32 v79, v92, v77
	s_and_saveexec_b64 s[4:5], vcc
	s_cbranch_execz .LBB1_18
	v_add_u32_e32 v92, v81, v82
	v_ashrrev_i32_e32 v93, 31, v92
	v_lshl_add_u64 v[92:93], v[92:93], 4, s[8:9]
	s_waitcnt lgkmcnt(2)
	v_pk_add_f32 v[72:73], v[72:73], v[74:75]
	s_waitcnt lgkmcnt(0)
	v_pk_add_f32 v[74:75], v[76:77], v[78:79]
	global_store_dwordx4 v[92:93], v[72:75], off
	s_branch .LBB1_18

.LBB1_52:
	s_or_b64 exec, exec, s[8:9]
	v_lshlrev_b32_e32 v1, 1, v0
	s_movk_i32 s8, 0xc4
	v_cmp_gt_u32_e64 s[10:11], s8, v0
	v_mov_b32_e32 v53, 0
	v_lshlrev_b32_e32 v56, 2, v1
	v_mov_b32_e32 v55, 0
	s_waitcnt lgkmcnt(0)
	s_barrier
	s_and_saveexec_b64 s[8:9], s[10:11]
	ds_read_b32 v55, v56 offset:4160
	s_or_b64 exec, exec, s[8:9]
	v_or_b32_e32 v54, 1, v1
	s_movk_i32 s8, 0x187
	v_cmp_gt_u32_e64 s[8:9], s8, v54
	s_and_saveexec_b64 s[12:13], s[8:9]
	ds_read_b32 v53, v56 offset:4164
	s_or_b64 exec, exec, s[12:13]
	s_waitcnt lgkmcnt(0)
	v_add_u32_e32 v56, v53, v55
	v_mov_b32_e32 v57, 0
	v_cmp_ne_u32_e64 s[12:13], 0, v0
	v_mov_b32_e32 v58, 0
	ds_write_b32 v40, v56
	s_waitcnt lgkmcnt(0)
	s_barrier
	s_and_saveexec_b64 s[14:15], s[12:13]
	v_add_u32_e32 v58, -4, v40
	ds_read_b32 v58, v58
	s_or_b64 exec, exec, s[14:15]
	s_waitcnt lgkmcnt(0)
	s_barrier
	ds_read_b32 v59, v40
	v_cmp_lt_u32_e64 s[12:13], 1, v0
	s_waitcnt lgkmcnt(0)
	v_add_u32_e32 v58, v59, v58
	ds_write_b32 v40, v58
	s_waitcnt lgkmcnt(0)
	s_barrier
	s_and_saveexec_b64 s[14:15], s[12:13]
	v_add_u32_e32 v57, -8, v40
	ds_read_b32 v57, v57
	s_or_b64 exec, exec, s[14:15]
	s_waitcnt lgkmcnt(0)
	s_barrier
	ds_read_b32 v58, v40
	v_cmp_lt_u32_e64 s[12:13], 3, v0
	s_waitcnt lgkmcnt(0)
	v_add_u32_e32 v57, v58, v57
	ds_write_b32 v40, v57
	v_mov_b32_e32 v57, 0
	v_mov_b32_e32 v58, 0
	s_waitcnt lgkmcnt(0)
	s_barrier
	s_and_saveexec_b64 s[14:15], s[12:13]
	v_add_u32_e32 v58, -16, v40
	ds_read_b32 v58, v58
	s_or_b64 exec, exec, s[14:15]
	s_waitcnt lgkmcnt(0)
	s_barrier
	ds_read_b32 v59, v40
	v_cmp_lt_u32_e64 s[12:13], 7, v0
	s_waitcnt lgkmcnt(0)
	v_add_u32_e32 v58, v59, v58
	ds_write_b32 v40, v58
	s_waitcnt lgkmcnt(0)
	s_barrier
	s_and_saveexec_b64 s[14:15], s[12:13]
	v_subrev_u32_e32 v57, 32, v40
	ds_read_b32 v57, v57
	s_or_b64 exec, exec, s[14:15]
	s_waitcnt lgkmcnt(0)
	s_barrier
	ds_read_b32 v58, v40
	v_cmp_lt_u32_e64 s[12:13], 15, v0
	s_waitcnt lgkmcnt(0)
	v_add_u32_e32 v57, v58, v57
	ds_write_b32 v40, v57
	v_mov_b32_e32 v57, 0
	v_mov_b32_e32 v58, 0
	s_waitcnt lgkmcnt(0)
	s_barrier
	s_and_saveexec_b64 s[14:15], s[12:13]
	v_subrev_u32_e32 v58, 64, v40
	ds_read_b32 v58, v58
	s_or_b64 exec, exec, s[14:15]
	s_waitcnt lgkmcnt(0)
	s_barrier
	ds_read_b32 v59, v40
	v_cmp_lt_u32_e64 s[12:13], 31, v0
	s_waitcnt lgkmcnt(0)
	v_add_u32_e32 v58, v59, v58
	ds_write_b32 v40, v58
	s_waitcnt lgkmcnt(0)
	s_barrier
	s_and_saveexec_b64 s[14:15], s[12:13]
	v_add_u32_e32 v57, 0xffffff80, v40
	ds_read_b32 v57, v57
	s_or_b64 exec, exec, s[14:15]
	s_waitcnt lgkmcnt(0)
	s_barrier
	ds_read_b32 v58, v40
	v_cmp_lt_u32_e64 s[12:13], 63, v0
	s_waitcnt lgkmcnt(0)
	v_add_u32_e32 v57, v58, v57
	ds_write_b32 v40, v57
	v_mov_b32_e32 v57, 0
	v_mov_b32_e32 v58, 0
	s_waitcnt lgkmcnt(0)
	s_barrier
	s_and_saveexec_b64 s[14:15], s[12:13]
	v_add_u32_e32 v58, 0xffffff00, v40
	ds_read_b32 v58, v58
	s_or_b64 exec, exec, s[14:15]
	s_waitcnt lgkmcnt(0)
	s_barrier
	ds_read_b32 v59, v40
	s_movk_i32 s12, 0x7f
	v_cmp_lt_u32_e64 s[12:13], s12, v0
	s_waitcnt lgkmcnt(0)
	v_add_u32_e32 v58, v59, v58
	ds_write_b32 v40, v58
	s_waitcnt lgkmcnt(0)
	s_barrier
	s_and_saveexec_b64 s[14:15], s[12:13]
	v_add_u32_e32 v57, 0xfffffe00, v40
	ds_read_b32 v57, v57
	s_or_b64 exec, exec, s[14:15]
	s_waitcnt lgkmcnt(0)
	s_barrier
	ds_read_b32 v58, v40
	s_waitcnt lgkmcnt(0)
	v_add_u32_e32 v57, v58, v57
	ds_write_b32 v40, v57
	s_waitcnt lgkmcnt(0)
	s_barrier
	ds_read_b32 v57, v40
	v_add_u32_e32 v40, v40, v34
	s_waitcnt lgkmcnt(0)
	s_barrier
	v_sub_u32_e32 v56, v57, v56
	s_and_saveexec_b64 s[12:13], s[10:11]
	s_cbranch_execz .LBB1_80
	v_mov_b32_e32 v60, v55
	v_mov_b32_e32 v61, v53
	v_lshlrev_b32_e32 v57, 8, v0
	global_atomic_add_x2 v[62:63], v57, v[60:61], s[16:17] sc0
	ds_write_b32 v40, v56 offset:1024
	v_add_u32_e32 v58, v56, v55
	s_and_saveexec_b64 s[14:15], s[8:9]
	ds_write_b32 v40, v58 offset:1028
	s_or_b64 exec, exec, s[14:15]
	s_waitcnt vmcnt(0)
	ds_write_b32 v40, v62 offset:2592
	s_and_saveexec_b64 s[14:15], s[8:9]
	ds_write_b32 v40, v63 offset:2596
.LBB1_80:
	s_or_b64 exec, exec, s[12:13]
	s_waitcnt lgkmcnt(0)
	s_barrier
	s_and_saveexec_b64 s[8:9], vcc
	s_cbranch_execz .LBB1_83
	v_or_b32_e32 v40, 0xffffff00, v0
	s_mov_b64 s[10:11], 0
	s_movk_i32 s12, 0x86

.LBB2_16:
	s_or_b64 exec, exec, s[4:5]
	s_lshl_b32 s3, s2, 2
	v_lshrrev_b32_e32 v14, 6, v0
	s_addk_i32 s3, 936
	v_add_u32_e32 v1, s3, v14
	s_movk_i32 s3, 0x186a
	v_cmp_gt_i32_e32 vcc, s3, v1
	s_waitcnt lgkmcnt(0)
	s_barrier
	s_and_saveexec_b64 s[6:7], vcc
	s_cbranch_execz .LBB2_21
	s_load_dwordx2 s[4:5], s[0:1], 0x38
	v_and_b32_e32 v80, 15, v0
	v_lshl_or_b32 v2, v1, 4, v80
	v_ashrrev_i32_e32 v3, 31, v2
	v_lshlrev_b64 v[2:3], 9, v[2:3]
	v_and_b32_e32 v66, 48, v0
	v_mov_b32_e32 v67, 0
	s_waitcnt lgkmcnt(0)
	v_lshl_add_u64 v[2:3], s[4:5], 0, v[2:3]
	v_lshl_add_u64 v[16:17], v[2:3], 0, v[66:67]
	global_load_dwordx4 v[38:41], v[16:17], off offset:448
	global_load_dwordx4 v[34:37], v[16:17], off offset:384
	global_load_dwordx4 v[26:29], v[16:17], off offset:320
	global_load_dwordx4 v[30:33], v[16:17], off offset:256
	global_load_dwordx4 v[6:9], v[16:17], off offset:192
	global_load_dwordx4 v[18:21], v[16:17], off offset:128
	global_load_dwordx4 v[2:5], v[16:17], off offset:64
	global_load_dwordx4 v[10:13], v[16:17], off
	s_load_dwordx2 s[8:9], s[0:1], 0x68
	s_load_dwordx2 s[10:11], s[0:1], 0x58
	v_and_b32_e32 v15, 63, v0
	s_movk_i32 s3, 0x1100
	v_cmp_gt_u32_e32 vcc, 16, v15
	v_mul_u32_u24_e32 v15, 0x110, v80
	v_mul_u32_u24_e32 v17, 0x1100, v14
	v_mad_u32_u24 v22, v14, s3, v15
	v_lshlrev_b32_e32 v16, 4, v80
	v_lshlrev_b32_e32 v14, 4, v14
	v_bfe_u32 v81, v0, 4, 2
	v_or_b32_e32 v24, v17, v16
	v_mov_b32_e32 v17, v67
	v_lshl_or_b32 v82, s2, 6, v14
	v_mbcnt_lo_u32_b32 v14, -1, 0
	s_waitcnt lgkmcnt(0)
	v_lshl_add_u64 v[70:71], s[10:11], 0, v[16:17]
	v_or_b32_e32 v17, 4, v81
	v_mbcnt_hi_u32_b32 v84, -1, v14
	v_lshlrev_b32_e32 v23, 3, v81
	v_mul_u32_u24_e32 v16, 0x110, v81
	v_mul_u32_u24_e32 v17, 0x110, v17
	v_and_b32_e32 v14, 64, v84
	v_lshl_add_u64 v[68:69], s[4:5], 0, v[66:67]
	v_or_b32_e32 v67, 0x3a80, v80
	s_mov_b64 s[10:11], 0
	s_movk_i32 s3, 0x1285
	s_movk_i32 s14, 0x1286
	v_add_u32_e32 v83, v66, v15
	v_xor_b32_e32 v85, 16, v84
	v_add_u32_e32 v86, 64, v14
	v_xor_b32_e32 v87, 32, v84
	v_add_u32_e32 v88, v22, v23
	v_add_u32_e32 v89, v24, v16
	v_add_u32_e32 v90, v24, v17
	s_waitcnt vmcnt(0)
	s_branch .LBB2_19
.LBB2_18:
	s_or_b64 exec, exec, s[12:13]
	v_cvt_pk_f16_f32 v41, v40, v41
	v_cvt_pk_f16_f32 v40, v38, v39
	v_cvt_pk_f16_f32 v38, v62, v63
	v_add_u32_e32 v62, 0x8800, v88
	v_cvt_pk_f16_f32 v37, v36, v37
	v_cvt_pk_f16_f32 v36, v34, v35
	v_cvt_pk_f16_f32 v35, v56, v57
	v_cvt_pk_f16_f32 v34, v54, v55
	ds_write2_b64 v62, v[36:37], v[34:35] offset0:8 offset1:12
	v_cvt_pk_f16_f32 v35, v48, v49
	v_cvt_pk_f16_f32 v34, v46, v47
	v_cvt_pk_f16_f32 v37, v52, v53
	v_cvt_pk_f16_f32 v36, v50, v51
	v_cvt_pk_f16_f32 v39, v64, v65
	ds_write2_b64 v62, v[34:35], v[36:37] offset0:16 offset1:20
	v_cvt_pk_f16_f32 v35, v44, v45
	v_cvt_pk_f16_f32 v34, v42, v43
	v_cvt_pk_f16_f32 v37, v60, v61
	v_cvt_pk_f16_f32 v36, v58, v59
	ds_write2_b64 v62, v[40:41], v[38:39] offset1:4
	ds_write2_b64 v62, v[34:35], v[36:37] offset0:24 offset1:28
	ds_read_b128 v[34:37], v89 offset:34816
	v_add_u32_e32 v44, v81, v82
	v_add_u32_e32 v38, 0x3a80, v44
	v_ashrrev_i32_e32 v39, 31, v38
	v_lshlrev_b64 v[38:39], 8, v[38:39]
	v_lshl_add_u64 v[42:43], v[70:71], 0, v[38:39]
	ds_read_b128 v[38:41], v90 offset:34816
	s_waitcnt lgkmcnt(1)
	global_store_dwordx4 v[42:43], v[34:37], off
	s_and_b64 s[4:5], exec, s[4:5]
	s_or_b64 s[10:11], s[4:5], s[10:11]
	v_add_u32_e32 v34, 0x3a84, v44
	v_ashrrev_i32_e32 v35, 31, v34
	v_lshlrev_b64 v[34:35], 8, v[34:35]
	v_lshl_add_u64 v[34:35], v[70:71], 0, v[34:35]
	s_waitcnt lgkmcnt(0)
	global_store_dwordx4 v[34:35], v[38:41], off
	ds_read_b128 v[34:37], v90 offset:35904
	v_add_u32_e32 v82, 0x5e40, v82
	v_add_u32_e32 v38, 0x3a88, v44
	v_ashrrev_i32_e32 v39, 31, v38
	v_lshlrev_b64 v[38:39], 8, v[38:39]
	v_lshl_add_u64 v[42:43], v[70:71], 0, v[38:39]
	ds_read_b128 v[38:41], v90 offset:36992
	s_waitcnt lgkmcnt(1)
	global_store_dwordx4 v[42:43], v[34:37], off
	s_nop 1
	v_add_u32_e32 v34, 0x3a8c, v44
	v_ashrrev_i32_e32 v35, 31, v34
	v_lshlrev_b64 v[34:35], 8, v[34:35]
	v_lshl_add_u64 v[34:35], v[70:71], 0, v[34:35]
	s_waitcnt lgkmcnt(0)
	global_store_dwordx4 v[34:35], v[38:41], off
	s_waitcnt vmcnt(5)
	v_mov_b64_e32 v[36:37], v[32:33]
	v_mov_b64_e32 v[34:35], v[30:31]
	v_mov_b64_e32 v[32:33], v[24:25]
	v_mov_b64_e32 v[30:31], v[22:23]
	s_waitcnt vmcnt(4)
	v_mov_b64_e32 v[40:41], v[28:29]
	v_mov_b64_e32 v[38:39], v[26:27]
	v_mov_b64_e32 v[28:29], v[16:17]
	v_mov_b64_e32 v[26:27], v[14:15]
	s_andn2_b64 exec, exec, s[10:11]
	s_cbranch_execz .LBB2_21
.LBB2_19:
	ds_read_b128 v[14:17], v83
	v_cvt_pk_f16_f32 v5, v4, v5
	v_cvt_pk_f16_f32 v4, v2, v3
	v_cvt_pk_f16_f32 v3, v12, v13
	v_cvt_pk_f16_f32 v2, v10, v11
	ds_read_b128 v[10:13], v83 offset:64
	ds_read_b128 v[22:25], v83 offset:4352
	ds_read_b128 v[42:45], v83 offset:4416
	ds_read_b128 v[46:49], v83 offset:8704
	ds_read_b128 v[50:53], v83 offset:8768
	ds_read_b128 v[54:57], v83 offset:13056
	ds_read_b128 v[58:61], v83 offset:13120
	ds_read_b128 v[62:65], v83 offset:17408
	ds_read_b128 v[72:75], v83 offset:17472
	ds_read_b128 v[76:79], v83 offset:21760
	ds_read_b128 v[92:95], v83 offset:21824
	ds_read_b128 v[96:99], v83 offset:26112
	ds_read_b128 v[100:103], v83 offset:26176
	ds_read_b128 v[104:107], v83 offset:30464
	ds_read_b128 v[110:113], v83 offset:30528
	v_mov_b32_e32 v91, v1
	v_add_u32_e32 v1, 0x5e4, v91
	v_cmp_gt_i32_e64 s[4:5], s14, v91
	s_waitcnt lgkmcnt(14)
	v_mfma_f32_16x16x32_f16 v[14:17], v[14:17], v[2:5], 0
	v_cvt_pk_f16_f32 v109, v8, v9
	v_cvt_pk_f16_f32 v108, v6, v7
	v_cvt_pk_f16_f32 v127, v40, v41
	s_waitcnt lgkmcnt(13)
	v_mfma_f32_16x16x32_f16 v[22:25], v[22:25], v[2:5], 0
	v_cvt_pk_f16_f32 v126, v38, v39
	v_cvt_pk_f16_f32 v125, v36, v37
	v_cvt_pk_f16_f32 v124, v34, v35
	s_waitcnt lgkmcnt(11)
	v_mfma_f32_16x16x32_f16 v[46:49], v[46:49], v[2:5], 0
	s_waitcnt lgkmcnt(9)
	v_mfma_f32_16x16x32_f16 v[54:57], v[54:57], v[2:5], 0
	s_waitcnt lgkmcnt(7)
	v_mfma_f32_16x16x32_f16 v[62:65], v[62:65], v[2:5], 0
	s_waitcnt lgkmcnt(5)
	v_mfma_f32_16x16x32_f16 v[76:79], v[76:79], v[2:5], 0
	s_waitcnt lgkmcnt(3)
	v_mfma_f32_16x16x32_f16 v[96:99], v[96:99], v[2:5], 0
	s_waitcnt lgkmcnt(1)
	v_mfma_f32_16x16x32_f16 v[114:117], v[104:107], v[2:5], 0
	v_cndmask_b32_e64 v2, v91, v1, s[4:5]
	v_lshl_or_b32 v2, v2, 4, v80
	v_ashrrev_i32_e32 v3, 31, v2
	v_lshlrev_b64 v[2:3], 9, v[2:3]
	v_cvt_pk_f16_f32 v107, v20, v21
	v_cvt_pk_f16_f32 v106, v18, v19
	v_lshl_add_u64 v[122:123], v[68:69], 0, v[2:3]
	v_cmp_lt_i32_e64 s[4:5], v85, v86
	v_mfma_f32_16x16x32_f16 v[118:121], v[10:13], v[106:109], v[14:17]
	global_load_dwordx4 v[10:13], v[122:123], off
	global_load_dwordx4 v[2:5], v[122:123], off offset:64
	global_load_dwordx4 v[18:21], v[122:123], off offset:128
	global_load_dwordx4 v[6:9], v[122:123], off offset:192
	v_cndmask_b32_e64 v34, v84, v85, s[4:5]
	v_lshlrev_b32_e32 v142, 2, v34
	v_mfma_f32_16x16x32_f16 v[42:45], v[42:45], v[106:109], v[22:25]
	s_nop 2
	global_load_dwordx4 v[22:25], v[122:123], off offset:256
	global_load_dwordx4 v[14:17], v[122:123], off offset:320
	v_cmp_lt_i32_e64 s[4:5], v87, v86
	v_mfma_f32_16x16x32_f16 v[46:49], v[50:53], v[106:109], v[46:49]
	s_nop 0
	v_cndmask_b32_e64 v143, v84, v87, s[4:5]
	v_cmp_lt_i32_e64 s[4:5], s3, v91
	v_mfma_f32_16x16x32_f16 v[50:53], v[58:61], v[106:109], v[54:57]
	v_mfma_f32_16x16x32_f16 v[54:57], v[72:75], v[106:109], v[62:65]
	ds_read_b128 v[72:75], v83 offset:128
	v_mfma_f32_16x16x32_f16 v[58:61], v[92:95], v[106:109], v[76:79]
	s_nop 0
	v_cvt_pk_f16_f32 v65, v28, v29
	v_cvt_pk_f16_f32 v64, v26, v27
	v_cvt_pk_f16_f32 v63, v32, v33
	v_mfma_f32_16x16x32_f16 v[76:79], v[100:103], v[106:109], v[96:99]
	ds_read_b128 v[92:95], v83 offset:4480
	v_cvt_pk_f16_f32 v62, v30, v31
	s_waitcnt lgkmcnt(2)
	v_mfma_f32_16x16x32_f16 v[96:99], v[110:113], v[106:109], v[114:117]
	ds_read_b128 v[100:103], v83 offset:8832
	ds_read_b128 v[104:107], v83 offset:192
	global_load_dwordx4 v[30:33], v[122:123], off offset:384
	global_load_dwordx4 v[26:29], v[122:123], off offset:448
	ds_read_b128 v[108:111], v83 offset:13184
	ds_read_b128 v[112:115], v83 offset:4544
	s_waitcnt lgkmcnt(5)
	v_mfma_f32_16x16x32_f16 v[72:75], v[72:75], v[62:65], v[118:121]
	s_waitcnt lgkmcnt(4)
	v_mfma_f32_16x16x32_f16 v[42:45], v[92:95], v[62:65], v[42:45]
	ds_read_b128 v[92:95], v83 offset:17536
	ds_read_b128 v[116:119], v83 offset:21888
	ds_read_b128 v[120:123], v83 offset:8896
	ds_read_b128 v[128:131], v83 offset:13248
	s_waitcnt lgkmcnt(7)
	v_mfma_f32_16x16x32_f16 v[46:49], v[100:103], v[62:65], v[46:49]
	ds_read_b128 v[100:103], v83 offset:26240
	s_waitcnt lgkmcnt(6)
	v_mfma_f32_16x16x32_f16 v[50:53], v[108:111], v[62:65], v[50:53]
	ds_read_b128 v[108:111], v83 offset:17600
	ds_read_b128 v[132:135], v83 offset:21952
	ds_read_b128 v[136:139], v83 offset:26304
	s_waitcnt lgkmcnt(7)
	v_mfma_f32_16x16x32_f16 v[92:95], v[92:95], v[62:65], v[54:57]
	s_waitcnt lgkmcnt(6)
	v_mfma_f32_16x16x32_f16 v[58:61], v[116:119], v[62:65], v[58:61]
	s_nop 0
	ds_read_b128 v[54:57], v83 offset:30592
	ds_read_b128 v[116:119], v83 offset:30656
	s_waitcnt lgkmcnt(5)
	v_mfma_f32_16x16x32_f16 v[76:79], v[100:103], v[62:65], v[76:79]
	v_mfma_f32_16x16x32_f16 v[38:41], v[104:107], v[124:127], v[72:75]
	s_nop 2
	ds_read_b128 v[72:75], v66 offset:52736
	ds_read_b128 v[100:103], v66 offset:52800
	ds_read_b128 v[104:107], v66 offset:52864
	s_nop 1
	v_mov_b32_e32 v140, v38
	v_mfma_f32_16x16x32_f16 v[34:37], v[120:123], v[124:127], v[46:49]
	ds_read_b128 v[120:123], v66 offset:52928
	s_waitcnt lgkmcnt(3)
	s_nop 0
	v_mov_b32_e32 v46, v72
	v_mfma_f32_16x16x32_f16 v[96:99], v[54:57], v[62:65], v[96:99]
	s_nop 2
	v_mov_b32_e32 v141, v34
	s_waitcnt lgkmcnt(1)
	v_mov_b32_e32 v47, v104
	v_pk_fma_f32 v[46:47], v[140:141], v[46:47], 0 op_sel_hi:[1,1,0]
	v_mfma_f32_16x16x32_f16 v[62:65], v[112:115], v[124:127], v[42:45]
	v_mov_b32_e32 v48, v39
	v_mov_b32_e32 v49, v35
	v_mov_b32_e32 v104, v73
	v_mfma_f32_16x16x32_f16 v[54:57], v[128:131], v[124:127], v[50:53]
	v_fma_f32 v42, v48, v104, v46
	v_fma_f32 v43, v49, v105, v47
	v_mov_b32_e32 v44, v40
	v_mov_b32_e32 v45, v36
	v_mov_b32_e32 v50, v74
	v_mov_b32_e32 v51, v106
	v_pk_fma_f32 v[42:43], v[44:45], v[50:51], v[42:43]
	v_mov_b32_e32 v44, v41
	v_mov_b32_e32 v45, v37
	v_mov_b32_e32 v106, v75
	v_pk_fma_f32 v[72:73], v[44:45], v[106:107], v[42:43]
	v_mfma_f32_16x16x32_f16 v[42:45], v[136:139], v[124:127], v[76:79]
	v_mov_b32_e32 v74, v62
	v_mov_b32_e32 v75, v54
	s_nop 0
	v_mov_b32_e32 v76, v100
	s_waitcnt lgkmcnt(0)
	v_mov_b32_e32 v77, v120
	v_pk_fma_f32 v[72:73], v[74:75], v[76:77], v[72:73]
	v_mov_b32_e32 v74, v63
	v_mov_b32_e32 v75, v55
	v_mov_b32_e32 v120, v101
	v_pk_fma_f32 v[72:73], v[74:75], v[120:121], v[72:73]
	v_mov_b32_e32 v74, v64
	v_mov_b32_e32 v75, v56
	v_mov_b32_e32 v76, v102
	v_mov_b32_e32 v77, v122
	v_pk_fma_f32 v[72:73], v[74:75], v[76:77], v[72:73]
	v_mov_b32_e32 v74, v65
	v_mov_b32_e32 v75, v57
	v_mov_b32_e32 v122, v103
	v_mfma_f32_16x16x32_f16 v[46:49], v[108:111], v[124:127], v[92:95]
	v_fma_f32 v100, v74, v122, v72
	v_fma_f32 v101, v75, v123, v73
	ds_read_b128 v[72:75], v66 offset:52992
	ds_read_b128 v[76:79], v66 offset:53056
	ds_read_b128 v[92:95], v66 offset:53120
	v_mov_b32_e32 v105, v42
	v_mfma_f32_16x16x32_f16 v[50:53], v[132:135], v[124:127], v[58:61]
	s_nop 0
	v_mov_b32_e32 v104, v46
	s_waitcnt lgkmcnt(2)
	v_mov_b32_e32 v106, v72
	s_waitcnt lgkmcnt(0)
	v_mov_b32_e32 v107, v92
	v_mfma_f32_16x16x32_f16 v[58:61], v[116:119], v[124:127], v[96:99]
	v_fma_f32 v104, v104, v106, 0
	v_fma_f32 v105, v105, v107, 0
	v_mov_b32_e32 v106, v47
	v_mov_b32_e32 v107, v43
	ds_read_b128 v[96:99], v66 offset:53184
	v_mov_b32_e32 v92, v73
	v_pk_fma_f32 v[72:73], v[106:107], v[92:93], v[104:105]
	v_mov_b32_e32 v92, v48
	v_mov_b32_e32 v93, v44
	v_mov_b32_e32 v104, v74
	v_mov_b32_e32 v105, v94
	v_pk_fma_f32 v[72:73], v[92:93], v[104:105], v[72:73]
	v_mov_b32_e32 v92, v49
	v_mov_b32_e32 v93, v45
	v_mov_b32_e32 v94, v75
	v_pk_fma_f32 v[72:73], v[92:93], v[94:95], v[72:73]
	v_mov_b32_e32 v74, v50
	v_mov_b32_e32 v75, v58
	v_mov_b32_e32 v92, v76
	s_waitcnt lgkmcnt(0)
	v_mov_b32_e32 v93, v96
	v_pk_fma_f32 v[72:73], v[74:75], v[92:93], v[72:73]
	v_mov_b32_e32 v74, v51
	v_mov_b32_e32 v75, v59
	v_mov_b32_e32 v96, v77
	v_pk_fma_f32 v[72:73], v[74:75], v[96:97], v[72:73]
	v_mov_b32_e32 v74, v52
	v_mov_b32_e32 v75, v60
	v_mov_b32_e32 v76, v78
	v_mov_b32_e32 v77, v98
	v_pk_fma_f32 v[72:73], v[74:75], v[76:77], v[72:73]
	v_mov_b32_e32 v74, v53
	v_mov_b32_e32 v75, v61
	v_mov_b32_e32 v98, v79
	v_pk_fma_f32 v[76:77], v[74:75], v[98:99], v[72:73]
	ds_bpermute_b32 v102, v142, v100
	ds_bpermute_b32 v103, v142, v101
	ds_bpermute_b32 v78, v142, v76
	ds_bpermute_b32 v79, v142, v77
	v_lshlrev_b32_e32 v92, 2, v143
	s_waitcnt lgkmcnt(2)
	v_pk_add_f32 v[72:73], v[100:101], v[102:103]
	ds_bpermute_b32 v74, v92, v72
	s_waitcnt lgkmcnt(1)
	v_pk_add_f32 v[76:77], v[76:77], v[78:79]
	ds_bpermute_b32 v75, v92, v73
	ds_bpermute_b32 v78, v92, v76
	ds_bpermute_b32 v79, v92, v77
	s_and_saveexec_b64 s[12:13], vcc
	s_cbranch_execz .LBB2_18
	v_add_u32_e32 v92, v67, v82
	v_ashrrev_i32_e32 v93, 31, v92
	v_lshl_add_u64 v[92:93], v[92:93], 4, s[8:9]
	s_waitcnt lgkmcnt(2)
	v_pk_add_f32 v[72:73], v[72:73], v[74:75]
	s_waitcnt lgkmcnt(0)
	v_pk_add_f32 v[74:75], v[76:77], v[78:79]
	global_store_dwordx4 v[92:93], v[72:75], off
	s_branch .LBB2_18

.LBB2_25:
	s_or_b64 exec, exec, s[4:5]
	v_lshlrev_b32_e32 v2, 1, v0
	v_or_b32_e32 v3, 1, v2
	s_movk_i32 s3, 0x187
	v_cmp_gt_u32_e32 vcc, s3, v3
	s_and_saveexec_b64 s[4:5], vcc
	s_cbranch_execz .LBB2_27
	v_lshlrev_b32_e32 v4, 8, v0
	s_waitcnt lgkmcnt(0)
	global_load_dword v4, v4, s[8:9] offset:4
.LBB2_27:
	s_or_b64 exec, exec, s[4:5]
	v_lshlrev_b32_e32 v8, 2, v0
	s_waitcnt vmcnt(0)
	v_add_u32_e32 v4, v4, v1
	v_mov_b32_e32 v5, 0
	v_cmp_ne_u32_e32 vcc, 0, v0
	v_add_u32_e32 v51, -4, v8
	v_mov_b32_e32 v6, 0
	ds_write_b32 v8, v4
	s_waitcnt lgkmcnt(0)
	s_barrier
	s_and_saveexec_b64 s[4:5], vcc
	ds_read_b32 v6, v51
	s_or_b64 exec, exec, s[4:5]
	s_waitcnt lgkmcnt(0)
	s_barrier
	ds_read_b32 v7, v8
	v_cmp_lt_u32_e64 s[52:53], 1, v0
	v_add_u32_e32 v52, -8, v8
	s_waitcnt lgkmcnt(0)
	v_add_u32_e32 v6, v7, v6
	ds_write_b32 v8, v6
	s_waitcnt lgkmcnt(0)
	s_barrier
	s_and_saveexec_b64 s[4:5], s[52:53]
	ds_read_b32 v5, v52
	s_or_b64 exec, exec, s[4:5]
	s_waitcnt lgkmcnt(0)
	s_barrier
	ds_read_b32 v6, v8
	v_cmp_lt_u32_e64 s[54:55], 3, v0
	v_add_u32_e32 v53, -16, v8
	s_waitcnt lgkmcnt(0)
	v_add_u32_e32 v5, v6, v5
	ds_write_b32 v8, v5
	v_mov_b32_e32 v5, 0
	v_mov_b32_e32 v6, 0
	s_waitcnt lgkmcnt(0)
	s_barrier
	s_and_saveexec_b64 s[4:5], s[54:55]
	ds_read_b32 v6, v53
	s_or_b64 exec, exec, s[4:5]
	s_waitcnt lgkmcnt(0)
	s_barrier
	ds_read_b32 v7, v8
	v_cmp_lt_u32_e64 s[56:57], 7, v0
	v_subrev_u32_e32 v54, 32, v8
	s_waitcnt lgkmcnt(0)
	v_add_u32_e32 v6, v7, v6
	ds_write_b32 v8, v6
	s_waitcnt lgkmcnt(0)
	s_barrier
	s_and_saveexec_b64 s[4:5], s[56:57]
	ds_read_b32 v5, v54
	s_or_b64 exec, exec, s[4:5]
	s_waitcnt lgkmcnt(0)
	s_barrier
	ds_read_b32 v6, v8
	v_cmp_lt_u32_e64 s[58:59], 15, v0
	v_subrev_u32_e32 v55, 64, v8
	s_waitcnt lgkmcnt(0)
	v_add_u32_e32 v5, v6, v5
	ds_write_b32 v8, v5
	v_mov_b32_e32 v5, 0
	v_mov_b32_e32 v6, 0
	s_waitcnt lgkmcnt(0)
	s_barrier
	s_and_saveexec_b64 s[4:5], s[58:59]
	ds_read_b32 v6, v55
	s_or_b64 exec, exec, s[4:5]
	s_waitcnt lgkmcnt(0)
	s_barrier
	ds_read_b32 v7, v8
	v_cmp_lt_u32_e64 s[60:61], 31, v0
	s_waitcnt lgkmcnt(0)
	v_add_u32_e32 v6, v7, v6
	ds_write_b32 v8, v6
	s_waitcnt lgkmcnt(0)
	s_barrier
	s_and_saveexec_b64 s[4:5], s[60:61]
	v_add_u32_e32 v5, 0xffffff80, v8
	ds_read_b32 v5, v5
	s_or_b64 exec, exec, s[4:5]
	s_waitcnt lgkmcnt(0)
	s_barrier
	ds_read_b32 v6, v8
	v_cmp_lt_u32_e64 s[62:63], 63, v0
	s_waitcnt lgkmcnt(0)
	v_add_u32_e32 v5, v6, v5
	ds_write_b32 v8, v5
	v_mov_b32_e32 v5, 0
	v_mov_b32_e32 v6, 0
	s_waitcnt lgkmcnt(0)
	s_barrier
	s_and_saveexec_b64 s[4:5], s[62:63]
	v_add_u32_e32 v6, 0xffffff00, v8
	ds_read_b32 v6, v6
	s_or_b64 exec, exec, s[4:5]
	s_waitcnt lgkmcnt(0)
	s_barrier
	ds_read_b32 v7, v8
	s_movk_i32 s3, 0x7f
	v_cmp_lt_u32_e64 s[64:65], s3, v0
	s_waitcnt lgkmcnt(0)
	v_add_u32_e32 v6, v7, v6
	ds_write_b32 v8, v6
	s_waitcnt lgkmcnt(0)
	s_barrier
	s_and_saveexec_b64 s[4:5], s[64:65]
	v_add_u32_e32 v5, 0xfffffe00, v8
	ds_read_b32 v5, v5
	s_or_b64 exec, exec, s[4:5]
	s_waitcnt lgkmcnt(0)
	s_barrier
	ds_read_b32 v6, v8
	s_load_dwordx2 s[10:11], s[0:1], 0x0
	v_cmp_eq_u32_e64 s[6:7], s2, v2
	v_cmp_eq_u32_e64 s[4:5], s2, v3
	s_or_b64 s[12:13], s[6:7], s[4:5]
	s_waitcnt lgkmcnt(0)
	v_add_u32_e32 v5, v6, v5
	ds_write_b32 v8, v5
	s_waitcnt lgkmcnt(0)
	s_barrier
	ds_read_b32 v5, v8
	s_waitcnt lgkmcnt(0)
	s_barrier
	s_and_saveexec_b64 s[6:7], s[12:13]
	v_cndmask_b32_e64 v1, 0, v1, s[4:5]
	v_sub_u32_e32 v1, v1, v4
	v_add_u32_e32 v1, v1, v5
	v_mov_b32_e32 v2, 0
	ds_write_b32 v2, v1 offset:2048
	s_or_b64 exec, exec, s[6:7]
	s_lshr_b32 s80, s2, 1
	s_lshl_b32 s80, s80, 6
	s_and_b32 s81, s2, 1
	s_or_b32 s80, s80, s81
	s_mov_b32 s81, 0
	s_lshl_b64 s[4:5], s[80:81], 2
	s_add_u32 s4, s8, s4
	v_mov_b32_e32 v1, 0
	s_addc_u32 s5, s9, s5
	ds_write_b32 v8, v1 offset:1024
	s_waitcnt lgkmcnt(0)
	s_barrier
	s_load_dword s3, s[4:5], 0x0
	ds_read_b32 v2, v1 offset:2048
	s_waitcnt lgkmcnt(0)
	s_cmpk_lt_i32 s3, 0x1801
	s_cbranch_scc1 .LBB2_47
	s_load_dword s81, s[8:9], 0xc380
